# routed-expert queues: overflow-candidate row counts read from a per-workgroup LDS copy (filled once per phase) instead of a global load per rejected position; router preload loads paired
# baseline (speedup 1.0000x reference)
.LBB0_1023:
	s_cmp_le_i32 s74, s2
	s_cselect_b64 s[0:1], -1, 0
	s_and_b64 s[0:1], s[0:1], s[8:9]
	v_writelane_b32 v255, s0, 3
	s_andn2_b64 vcc, exec, s[0:1]
	s_nop 0
	v_writelane_b32 v255, s1, 4
	s_cbranch_vccnz .LBB0_1223
	v_readlane_b32 s0, v254, 41
	s_nop 1
	v_mov_b32_e32 v0, s0
	s_waitcnt vmcnt(0)
	ds_read_b64 v[2:3], v0
	v_mbcnt_lo_u32_b32 v0, -1, 0
	v_mbcnt_hi_u32_b32 v0, -1, v0
	v_readlane_b32 s0, v253, 0
	s_waitcnt lgkmcnt(0)
	v_readfirstlane_b32 s12, v2
	v_add_u32_e32 v0, s0, v0
	v_readlane_b32 s0, v254, 50
	v_readfirstlane_b32 s13, v3
	s_nop 0
	v_mov_b32_e32 v2, s0
	ds_read_b128 v[2:5], v2
	v_readlane_b32 s0, v254, 51
	v_readfirstlane_b32 s2, v0
	s_waitcnt lgkmcnt(0)
	v_readfirstlane_b32 s9, v2
	v_mov_b32_e32 v2, s0
	v_readfirstlane_b32 s11, v3
	ds_read_b64 v[2:3], v2
	s_movk_i32 s0, 0x100
	v_readfirstlane_b32 s14, v4
	v_readfirstlane_b32 s15, v5
	v_cmp_gt_i32_e32 vcc, s0, v0
	s_waitcnt lgkmcnt(0)
	v_readfirstlane_b32 s3, v2
	v_readfirstlane_b32 s8, v3
	s_and_saveexec_b64 s[0:1], vcc
	s_cbranch_execz .LBB0_1026
	v_readlane_b32 s16, v254, 60
	v_readlane_b32 s17, v254, 61
	s_lshl_b32 s56, s16, 10
	s_lshl_b64 s[16:17], s[56:57], 2
	s_add_u32 s14, s14, s16
	s_addc_u32 s15, s15, s17
	v_lshlrev_b32_e32 v2, 2, v0
	s_add_u32 s16, s9, s16
	v_ashrrev_i32_e32 v3, 31, v2
	s_addc_u32 s17, s11, s17
	v_lshlrev_b64 v[6:7], 2, v[2:3]
	v_lshl_add_u64 v[2:3], s[16:17], 0, v[6:7]
	global_load_dwordx4 v[2:5], v[2:3], off
	v_lshl_add_u64 v[10:11], s[14:15], 0, v[6:7]
	global_load_dwordx4 v[10:13], v[10:11], off
	v_lshl_add_u32 v8, v0, 4, 0
	v_add_u32_e32 v9, 0x17000, v8
	v_add_u32_e32 v6, 0x18000, v8
	s_waitcnt vmcnt(1)
	ds_write_b128 v9, v[2:5]
	s_waitcnt vmcnt(0)
	ds_write_b128 v6, v[10:13]

.LBB0_1279:
	s_cmp_le_i32 s74, s2
	s_cselect_b64 s[2:3], -1, 0
	s_and_b64 s[0:1], s[2:3], s[0:1]
	v_writelane_b32 v255, s0, 11
	s_andn2_b64 vcc, exec, s[0:1]
	s_nop 0
	v_writelane_b32 v255, s1, 12
	s_cbranch_vccnz .LBB0_1346
	v_readlane_b32 s0, v254, 41
	v_readlane_b32 s2, v254, 60
	v_readlane_b32 s3, v254, 61
	v_mov_b32_e32 v0, s0
	s_waitcnt vmcnt(0)
	ds_read_b64 v[2:3], v0
	s_mov_b32 s3, s57
	s_lshl_b32 s56, s2, 13
	s_lshl_b32 s0, s2, 8
	v_writelane_b32 v254, s2, 60
	s_waitcnt lgkmcnt(0)
	v_readfirstlane_b32 s15, v2
	s_lshl_b64 s[8:9], s[56:57], 2
	v_writelane_b32 v254, s3, 61
	s_lshl_b64 s[2:3], s[2:3], 28
	v_readfirstlane_b32 s16, v3
	s_add_u32 s8, s15, s8
	v_readlane_b32 s11, v253, 0
	s_addc_u32 s9, s16, s9
	v_mbcnt_lo_u32_b32 v0, -1, 0
	v_mbcnt_hi_u32_b32 v0, -1, v0
	s_mov_b32 s1, s57
	v_add_u32_e32 v231, s11, v0
	s_add_u32 s50, s8, 0x10000
	v_readfirstlane_b32 s8, v231
	s_addc_u32 s51, s9, 0
	s_ashr_i32 s9, s8, 6
	s_lshl_b64 s[18:19], s[0:1], 2
	s_add_u32 s0, s15, s18
	v_writelane_b32 v255, s18, 13
	s_addc_u32 s1, s16, s19
	s_add_u32 s52, s0, 0xa000
	s_addc_u32 s53, s1, 0
	v_readlane_b32 s11, v254, 53
	v_writelane_b32 v255, s19, 14
	s_add_u32 s0, s15, 0x2e3e0000
	v_mov_b32_e32 v0, s11
	v_writelane_b32 v255, s0, 15
	s_addc_u32 s0, s16, 0
	ds_read_b128 v[2:5], v0
	s_add_u32 s54, s15, 0x4ffe0a00
	s_addc_u32 s55, s16, 0
	s_add_u32 s58, s15, 0x2f3e0000
	v_writelane_b32 v255, s0, 16
	s_addc_u32 s59, s16, 0
	s_ashr_i32 s0, s8, 7
	s_and_b32 s1, s9, 1
	v_writelane_b32 v255, s15, 17
	s_lshl_b32 s28, s0, 5
	s_lshl_b32 s15, s1, 5
	s_waitcnt lgkmcnt(0)
	v_readfirstlane_b32 s11, v2
	v_readfirstlane_b32 s13, v4
	s_cmp_lt_i32 s0, 2
	v_readfirstlane_b32 s12, v3
	v_readfirstlane_b32 s14, v5
	s_cselect_b32 s11, s11, s13
	s_cselect_b32 s0, s12, s14
	s_add_u32 s2, s11, s2
	v_writelane_b32 v255, s16, 18
	s_addc_u32 s0, s0, s3
	s_lshl_b32 s3, s9, 8
	v_writelane_b32 v255, s15, 5
	s_add_i32 s3, s3, 0
	v_writelane_b32 v255, s3, 7
	s_and_b32 s3, s8, 0x80
	s_add_u32 s2, s2, s3
	s_addc_u32 s0, s0, 0
	s_and_b32 s83, s8, 0xffffffc0
	v_writelane_b32 v255, s2, 19
	s_lshl_b32 s2, s83, 2
	s_add_i32 s87, s2, 0
	s_ashr_i32 s2, s8, 8
	v_writelane_b32 v255, s0, 20
	s_lshl_b32 s0, s9, 5
	s_lshl_b32 s3, s2, 13
	s_and_b32 s0, s0, 0xffffff80
	s_add_i32 s3, s3, 0
	s_lshl_b32 s1, s1, 12
	s_add_i32 s0, s0, 0
	s_add_i32 s78, s3, s1
	v_writelane_b32 v255, s0, 9
	s_and_b32 s0, s9, 3
	s_or_b32 s80, s83, 32
	s_add_i32 s78, s78, 0x10000
	s_cmp_gt_u32 s0, 1
	s_cselect_b64 s[60:61], -1, 0
	s_cmp_lt_u32 s0, 2
	s_mul_i32 s33, s0, 0x1200
	s_cselect_b64 s[62:63], -1, 0
	s_lshl_b32 s64, s0, 5
	s_lshl_b32 s0, s9, 4
	s_and_b32 s0, s0, 16
	v_cmp_eq_u32_e64 s[18:19], 0, v231
	v_writelane_b32 v255, s0, 3
	s_lshl_b32 s1, s2, 7
	v_writelane_b32 v255, s18, 21
	s_add_i32 s3, s1, 0
	s_mov_b32 s65, s57
	v_writelane_b32 v255, s19, 22
	s_mov_b64 s[46:47], exec
	s_mov_b64 exec, -1
	v_cmp_gt_u32_e32 vcc, 0x100, v231
	s_and_saveexec_b64 s[38:39], vcc
	v_lshlrev_b32_e32 v5, 7, v231
	global_load_dword v6, v5, s[50:51]
	v_lshlrev_b32_e32 v5, 2, v231
	v_add_u32_e32 v5, 0x249f0, v5
	s_waitcnt vmcnt(0)
	ds_write_b32 v5, v6
	s_waitcnt lgkmcnt(0)
	s_mov_b64 exec, s[46:47]
	s_branch .LBB0_1283

.LBB0_1288:
	s_or_b64 exec, exec, s[12:13]
	s_waitcnt vmcnt(0)
	v_readfirstlane_b32 s2, v2
	s_mov_b64 s[14:15], -1
	s_nop 0
	v_add_u32_e32 v2, s2, v0
	v_add_u32_e32 v0, 0xffffff00, v2
	s_movk_i32 s2, 0x400
	v_cmp_gt_u32_e32 vcc, s2, v0
	s_and_saveexec_b64 s[12:13], vcc
	s_cbranch_execz .LBB0_1285
	v_lshrrev_b32_e32 v0, 2, v2
	v_lshlrev_b32_e32 v0, 2, v0
	v_add_u32_e32 v0, 0x248f0, v0
	ds_read_b32 v0, v0
	s_movk_i32 s2, 0x240
	s_waitcnt lgkmcnt(0)
	v_cmp_lt_i32_e32 vcc, s2, v0
	s_orn2_b64 s[14:15], vcc, exec
	s_branch .LBB0_1285

.LBB0_1402:
	s_cmp_le_i32 s74, s2
	s_cselect_b64 s[2:3], -1, 0
	s_and_b64 s[8:9], s[2:3], s[0:1]
	s_andn2_b64 vcc, exec, s[8:9]
	s_cbranch_vccnz .LBB0_1456
	v_readlane_b32 s2, v254, 60
	v_readlane_b32 s0, v254, 41
	v_readlane_b32 s3, v254, 61
	s_mov_b32 s3, s57
	v_mov_b32_e32 v0, s0
	s_waitcnt vmcnt(0)
	ds_read_b64 v[2:3], v0
	s_lshl_b32 s56, s2, 13
	s_lshl_b64 s[12:13], s[2:3], 28
	v_writelane_b32 v254, s2, 60
	v_readlane_b32 s11, v253, 0
	v_mbcnt_lo_u32_b32 v0, -1, 0
	v_mbcnt_hi_u32_b32 v0, -1, v0
	s_lshl_b32 s0, s2, 8
	v_writelane_b32 v254, s3, 61
	v_add_u32_e32 v231, s11, v0
	v_readlane_b32 s11, v254, 55
	s_waitcnt lgkmcnt(0)
	v_readfirstlane_b32 s2, v2
	v_readfirstlane_b32 s3, v3
	v_mov_b32_e32 v0, s11
	ds_read_b64 v[2:3], v0
	s_or_b32 s14, s0, 64
	s_lshl_b64 s[0:1], s[56:57], 2
	s_add_u32 s0, s2, s0
	s_addc_u32 s1, s3, s1
	s_add_u32 s0, s0, 0x10000
	v_readfirstlane_b32 s33, v231
	s_addc_u32 s1, s1, 0
	s_ashr_i32 s25, s33, 6
	s_waitcnt lgkmcnt(0)
	v_readfirstlane_b32 s11, v2
	s_mov_b32 s15, s57
	v_readfirstlane_b32 s16, v3
	s_add_u32 s27, s11, s12
	s_addc_u32 s34, s16, s13
	s_lshl_b64 s[14:15], s[14:15], 2
	s_add_u32 s11, s2, s14
	s_addc_u32 s12, s3, s15
	s_add_u32 s16, s11, 0xa000
	s_addc_u32 s17, s12, 0
	s_add_u32 s11, s2, 0x2e3e0000
	s_addc_u32 s26, s3, 0
	s_add_u32 s18, s2, 0x2e360000
	s_addc_u32 s19, s3, 0
	s_add_u32 s30, s2, 0x2f3e0000
	s_addc_u32 s31, s3, 0
	s_add_u32 s12, s2, 0x33be0200
	s_addc_u32 s13, s3, 0
	s_lshl_b32 s28, s25, 4
	v_bfe_u32 v3, v231, 3, 3
	v_and_b32_e32 v2, 7, v231
	v_and_or_b32 v3, s28, 16, v3
	s_andn2_b32 s28, s28, 31
	v_lshlrev_b32_e32 v4, 4, v2
	v_or_b32_e32 v2, s28, v2
	s_movk_i32 s35, 0x90
	s_ashr_i32 s29, s28, 31
	v_mul_lo_u32 v2, v2, s35
	s_lshl_b32 s35, s25, 8
	s_add_i32 s35, s35, 0
	s_lshl_b64 s[28:29], s[28:29], 2
	s_add_u32 s27, s27, s28
	s_addc_u32 s28, s34, s29
	s_lshl_b32 s34, s25, 5
	v_and_b32_e32 v0, 31, v231
	s_and_b32 s29, s34, 0xffffff80
	v_and_b32_e32 v232, 32, v231
	v_lshl_add_u32 v234, v3, 2, v2
	v_mul_u32_u24_e32 v2, 0x48, v0
	v_lshlrev_b32_e32 v0, 2, v0
	s_add_i32 s29, s29, 0
	s_andn2_b32 s33, s33, 63
	s_and_b32 s38, s25, 3
	v_cmp_eq_u32_e64 s[40:41], 0, v231
	v_lshl_or_b32 v233, v3, 13, v4
	v_add_lshl_u32 v235, v2, v232, 1
	v_add_u32_e32 v236, s35, v0
	v_add_u32_e32 v237, s29, v0
	s_mulk_i32 s38, 0x1200
	s_or_b32 s39, s33, 32
	s_and_b32 s34, s34, 0x60
	s_mov_b32 s35, s57
	s_mov_b64 s[48:49], exec
	s_mov_b64 exec, -1
	v_cmp_gt_u32_e32 vcc, 0x100, v231
	s_and_saveexec_b64 s[42:43], vcc
	v_lshlrev_b32_e32 v5, 7, v231
	global_load_dword v6, v5, s[0:1]
	v_lshlrev_b32_e32 v5, 2, v231
	v_add_u32_e32 v5, 0x249f0, v5
	s_waitcnt vmcnt(0)
	ds_write_b32 v5, v6
	s_waitcnt lgkmcnt(0)
	s_mov_b64 exec, s[48:49]
	s_branch .LBB0_1406

.LBB0_1411:
	s_or_b64 exec, exec, s[44:45]
	s_waitcnt vmcnt(0)
	v_readfirstlane_b32 s25, v2
	s_mov_b64 s[46:47], -1
	s_nop 0
	v_add_u32_e32 v2, s25, v0
	v_add_u32_e32 v0, 0xffffff00, v2
	s_movk_i32 s25, 0x400
	v_cmp_gt_u32_e32 vcc, s25, v0
	s_and_saveexec_b64 s[44:45], vcc
	s_cbranch_execz .LBB0_1408
	v_lshrrev_b32_e32 v0, 2, v2
	v_lshlrev_b32_e32 v0, 2, v0
	v_add_u32_e32 v0, 0x248f0, v0
	ds_read_b32 v0, v0
	s_movk_i32 s25, 0x240
	s_waitcnt lgkmcnt(0)
	v_cmp_lt_i32_e32 vcc, s25, v0
	s_orn2_b64 s[46:47], vcc, exec
	s_branch .LBB0_1408
